# in-proj gate epilogue: the unit's 1 KB gate-bias tile is fetched by one LDS-DMA per wave at the top of the unit (ahead of its K-loop) and read from LDS in the epilogue, so the epilogue no longer start
# baseline (speedup 1.0000x reference)
;     __device__ __forceinline__ bool next(int i, gm::GUnit& u) const {
;         const int L = i * G + c, nlat = 256 * 16, nproj = nlat + (l == 0 ? 8 * 16 : 8 * 4), ngate = (l == 0 ? 264 : 256) * 16;
;         if (L >= nproj + ngate) return false;
;         int pm, pn, sub = 0;
;         if (L < nlat) grouped_order(L, 256, 16, pm, pn);
;         else if (L < nproj) { const int r = L - nlat; if (l == 0) { pm = 256 + (r >> 4); pn = r & 15; } else { pm = 256 + (r >> 2); pn = 2 + (r & 3); } }
;         else { grouped_order(L - nproj, l == 0 ? 264 : 256, 16, pm, pn); sub = 1; }
.LBB0_238:
	s_lshl_b32 s22, s74, 10
	s_add_u32 s22, s88, s22
	s_addc_u32 s23, s89, 0
	v_and_b32_e32 v234, 63, v0
	v_lshlrev_b32_e32 v234, 4, v234
	v_readfirstlane_b32 s101, v0
	s_nop 3
	s_lshl_b32 s101, s101, 4
	s_add_i32 m0, s101, 0x20000
	s_nop 0
	global_load_lds_dwordx4 v234, s[22:23]
	s_add_i32 s85, s85, 1
	s_mul_i32 s1, s85, s96
	v_readlane_b32 s22, v254, 62
	s_add_i32 s1, s1, s22
	s_cmp_lt_i32 s1, s31
	s_cselect_b64 s[78:79], -1, 0
	s_cmp_ge_i32 s1, s31
	s_cselect_b64 s[52:53], -1, 0
	s_and_b64 vcc, exec, s[52:53]
	v_readlane_b32 s23, v254, 63
	s_cbranch_vccnz .LBB0_252
	s_cmpk_gt_i32 s1, 0xfff
	s_mov_b64 s[24:25], -1
	s_cbranch_scc0 .LBB0_249
	s_cmp_ge_u32 s1, s58
	s_cbranch_scc0 .LBB0_242
	s_lshl_b32 s7, s1, 1
	s_sub_i32 s2, s1, s58
	s_and_b32 s7, s7, 14
	s_mul_i32 s7, s7, s90
	s_lshr_b32 s2, s2, 3
	s_add_i32 s7, s7, s2
	s_lshr_b32 s2, s7, 4
	s_and_b32 s2, s2, 0x1fffff8
	s_sub_i32 s22, s90, s2
	s_min_i32 s24, s22, 8
	s_sext_i32_i8 s22, s24
	v_cvt_f32_i32_e32 v2, s22
	s_and_b32 s7, s7, 0x7f
	v_cvt_f32_ubyte0_e32 v4, s7
	s_ashr_i32 s22, s22, 30
	v_rcp_iflag_f32_e32 v3, v2
	s_or_b32 s25, s22, 1
	v_mul_f32_e32 v3, v4, v3
	v_trunc_f32_e32 v3, v3
	v_fma_f32 v4, -v3, v2, v4
	v_cvt_i32_f32_e32 v3, v3
	v_cmp_ge_f32_e64 s[22:23], |v4|, |v2|
	s_and_b64 s[22:23], s[22:23], exec
	s_cselect_b32 s22, s25, 0
	v_readfirstlane_b32 s23, v3
	s_add_i32 s22, s23, s22
	s_sext_i32_i8 s54, s22
	s_mul_i32 s22, s22, s24
	s_sub_i32 s7, s7, s22
	s_and_b32 s7, s7, 0xff
	s_add_i32 s66, s2, s7
	s_mov_b64 s[24:25], 0

;     __device__ __forceinline__ void operator()(const AccT& acc, const gm::GUnit& u, int wr, int wc, int fr, int fq) const {
;     ...
;         if (u.sub == 1) {
;             const float* bp = bg + u.pn * 256 + wc * 32 + 8 * fq;
;             f32x4 bb[2][2];
; #pragma unroll
;             for (int bj = 0; bj < 2; ++bj) { bb[bj][0] = *(const f32x4*)(bp + bj * 128); bb[bj][1] = *(const f32x4*)(bp + bj * 128 + 4); }
;             __builtin_amdgcn_sched_barrier(0);
; #pragma unroll
;             for (int bj = 0; bj < 2; ++bj) {
;                 const f32x4 b0 = bb[bj][0], b1 = bb[bj][1];
; #pragma unroll
;                 for (int ai = 0; ai < 2; ++ai)
; #pragma unroll
;                     for (int m = 0; m < 4; ++m) {
;                         const int row = u.pm * 256 + ai * 128 + wr * 64 + m * 16 + fr;
;                         f32x4 v0 = (acc[ai][bj][m][0] + b0) * -1.4426950408889634f, v1 = (acc[ai][bj][m][1] + b1) * -1.4426950408889634f;
; #pragma unroll
;                         for (int j = 0; j < 4; ++j) { v0[j] = __builtin_amdgcn_exp2f(v0[j]); v1[j] = __builtin_amdgcn_exp2f(v1[j]); }
;                         v0 = v0 + 1.f; v1 = v1 + 1.f;
; #pragma unroll
;                         for (int j = 0; j < 4; ++j) { v0[j] = __builtin_amdgcn_rcpf(v0[j]); v1[j] = __builtin_amdgcn_rcpf(v1[j]); }
;                         v0 = v0 * 255.f + 0.5f; v1 = v1 * 255.f + 0.5f;
;                         unsigned q[8];
; #pragma unroll
;                         for (int j = 0; j < 4; ++j) { q[j] = max((unsigned)v0[j], 1u); q[4 + j] = max((unsigned)v1[j], 1u); }
;                         u32x2 w; w.x = q[0] | (q[1] << 8) | (q[2] << 16) | (q[3] << 24); w.y = q[4] | (q[5] << 8) | (q[6] << 16) | (q[7] << 24);
;                         *(u32x2*)(G8 + (size_t)row * INW + u.pn * 256 + bj * 128 + wc * 32 + 8 * fq) = w;
;                     }
.LBB0_263:
	s_and_b64 vcc, exec, s[8:9]
	s_cbranch_vccz .LBB0_237
	s_lshl_b32 s18, s74, 8
	s_ashr_i32 s19, s18, 31
	v_lshlrev_b32_e32 v148, 3, v203
	v_ashrrev_i32_e32 v149, 31, v148
	v_readfirstlane_b32 s0, v0
	s_nop 3
	s_lshl_b32 s0, s0, 4
	s_add_i32 s0, s0, 0x20000
	v_lshl_add_u32 v134, v203, 5, s0
	ds_read_b128 v[142:145], v134
	ds_read_b128 v[138:141], v134 offset:16
	ds_read_b128 v[130:133], v134 offset:528
	ds_read_b128 v[134:137], v134 offset:512
	s_waitcnt lgkmcnt(0)
	v_pk_add_f32 v[122:123], v[122:123], v[138:139]
	v_pk_add_f32 v[126:127], v[126:127], v[142:143]
	v_pk_add_f32 v[124:125], v[124:125], v[140:141]
	v_pk_mul_f32 v[122:123], v[122:123], s[6:7] op_sel_hi:[1,0]
	v_pk_mul_f32 v[126:127], v[126:127], s[6:7] op_sel_hi:[1,0]
	v_pk_mul_f32 v[124:125], v[124:125], s[6:7] op_sel_hi:[1,0]
	v_exp_f32_e32 v122, v122
	v_exp_f32_e32 v123, v123
	v_exp_f32_e32 v126, v126
	v_exp_f32_e32 v127, v127
	v_exp_f32_e32 v124, v124
	v_exp_f32_e32 v125, v125
	v_pk_add_f32 v[114:115], v[114:115], v[138:139]
	v_pk_add_f32 v[128:129], v[128:129], v[144:145]
	v_pk_mul_f32 v[114:115], v[114:115], s[6:7] op_sel_hi:[1,0]
	v_pk_add_f32 v[122:123], v[122:123], 1.0 op_sel_hi:[1,0]
	v_exp_f32_e32 v114, v114
	v_exp_f32_e32 v115, v115
	v_pk_mul_f32 v[128:129], v[128:129], s[6:7] op_sel_hi:[1,0]
	v_pk_add_f32 v[126:127], v[126:127], 1.0 op_sel_hi:[1,0]
	v_pk_add_f32 v[124:125], v[124:125], 1.0 op_sel_hi:[1,0]
	v_rcp_f32_e32 v122, v122
	v_rcp_f32_e32 v123, v123
	v_exp_f32_e32 v128, v128
	v_exp_f32_e32 v129, v129
	v_rcp_f32_e32 v126, v126
	v_rcp_f32_e32 v127, v127
	v_rcp_f32_e32 v124, v124
	v_rcp_f32_e32 v125, v125
	v_pk_add_f32 v[120:121], v[120:121], v[144:145]
	v_pk_add_f32 v[116:117], v[116:117], v[140:141]
	v_pk_mul_f32 v[120:121], v[120:121], s[6:7] op_sel_hi:[1,0]
	v_pk_mul_f32 v[116:117], v[116:117], s[6:7] op_sel_hi:[1,0]
	v_pk_add_f32 v[114:115], v[114:115], 1.0 op_sel_hi:[1,0]
	v_exp_f32_e32 v120, v120
	v_exp_f32_e32 v121, v121
	v_exp_f32_e32 v116, v116
	v_exp_f32_e32 v117, v117
	v_rcp_f32_e32 v114, v114
	v_fma_f32 v122, v122, s33, 0.5
	v_fma_f32 v123, v123, s33, 0.5
	v_pk_add_f32 v[128:129], v[128:129], 1.0 op_sel_hi:[1,0]
	v_fma_f32 v126, v126, s33, 0.5
	v_cvt_u32_f32_e32 v122, v122
	v_fma_f32 v127, v127, s33, 0.5
	v_cvt_u32_f32_e32 v123, v123
	v_fma_f32 v124, v124, s33, 0.5
	v_fma_f32 v125, v125, s33, 0.5
	v_pk_add_f32 v[118:119], v[118:119], v[142:143]
	v_rcp_f32_e32 v128, v128
	v_rcp_f32_e32 v129, v129
	v_cvt_u32_f32_e32 v126, v126
	v_cvt_u32_f32_e32 v127, v127
	v_cvt_u32_f32_e32 v124, v124
	v_cvt_u32_f32_e32 v125, v125
	v_pk_mul_f32 v[118:119], v[118:119], s[6:7] op_sel_hi:[1,0]
	v_pk_add_f32 v[120:121], v[120:121], 1.0 op_sel_hi:[1,0]
	v_exp_f32_e32 v118, v118
	v_exp_f32_e32 v119, v119
	v_pk_add_f32 v[116:117], v[116:117], 1.0 op_sel_hi:[1,0]
	v_rcp_f32_e32 v115, v115
	v_fma_f32 v114, v114, s33, 0.5
	s_lshl_b32 s0, s72, 8
	v_rcp_f32_e32 v120, v120
	v_rcp_f32_e32 v116, v116
	v_rcp_f32_e32 v117, v117
	v_cvt_u32_f32_e32 v114, v114
	v_pk_add_f32 v[106:107], v[106:107], v[138:139]
	v_max_u32_e32 v122, 1, v122
	v_max_u32_e32 v123, 1, v123
	s_add_i32 s0, s0, s82
	v_pk_mul_f32 v[106:107], v[106:107], s[6:7] op_sel_hi:[1,0]
	v_max_u32_e32 v126, 1, v126
	v_max_u32_e32 v127, 1, v127
	v_fma_f32 v128, v128, s33, 0.5
	v_fma_f32 v129, v129, s33, 0.5
	v_max_u32_sdwa v150, v124, v228 dst_sel:WORD_1 dst_unused:UNUSED_PAD src0_sel:DWORD src1_sel:DWORD
	v_max_u32_sdwa v125, v125, v228 dst_sel:BYTE_3 dst_unused:UNUSED_PAD src0_sel:DWORD src1_sel:DWORD
	v_add_u32_e32 v124, s0, v201
	v_lshl_or_b32 v122, v123, 8, v122
	v_exp_f32_e32 v106, v106
	v_exp_f32_e32 v107, v107
	v_cvt_u32_f32_e32 v128, v128
	v_cvt_u32_f32_e32 v129, v129
	v_lshl_or_b32 v126, v127, 8, v126
	v_or3_b32 v127, v122, v150, v125
	v_ashrrev_i32_e32 v125, 31, v124
	v_pk_add_f32 v[118:119], v[118:119], 1.0 op_sel_hi:[1,0]
	v_fma_f32 v115, v115, s33, 0.5
	v_lshlrev_b64 v[122:123], 12, v[124:125]
	v_rcp_f32_e32 v118, v118
	v_rcp_f32_e32 v119, v119
	v_cvt_u32_f32_e32 v115, v115
	v_max_u32_e32 v125, 1, v114
	v_fma_f32 v114, v120, s33, 0.5
	v_fma_f32 v116, v116, s33, 0.5
	v_fma_f32 v117, v117, s33, 0.5
	v_lshl_add_u64 v[122:123], s[46:47], 0, v[122:123]
	v_rcp_f32_e32 v121, v121
	v_cvt_u32_f32_e32 v114, v114
	v_cvt_u32_f32_e32 v116, v116
	v_cvt_u32_f32_e32 v117, v117
	v_pk_add_f32 v[112:113], v[112:113], v[144:145]
	v_pk_add_f32 v[108:109], v[108:109], v[140:141]
	v_lshl_add_u64 v[122:123], v[122:123], 0, s[18:19]
	v_pk_mul_f32 v[112:113], v[112:113], s[6:7] op_sel_hi:[1,0]
	v_pk_mul_f32 v[108:109], v[108:109], s[6:7] op_sel_hi:[1,0]
	v_pk_add_f32 v[106:107], v[106:107], 1.0 op_sel_hi:[1,0]
	v_max_u32_sdwa v128, v128, v228 dst_sel:WORD_1 dst_unused:UNUSED_PAD src0_sel:DWORD src1_sel:DWORD
	v_max_u32_sdwa v129, v129, v228 dst_sel:BYTE_3 dst_unused:UNUSED_PAD src0_sel:DWORD src1_sel:DWORD
	v_lshl_add_u64 v[122:123], v[122:123], 0, s[48:49]
	v_exp_f32_e32 v112, v112
	v_exp_f32_e32 v113, v113
	v_exp_f32_e32 v108, v108
	v_exp_f32_e32 v109, v109
	v_rcp_f32_e32 v106, v106
	v_or3_b32 v126, v126, v128, v129
	v_lshl_add_u64 v[122:123], v[122:123], 0, v[148:149]
	v_fma_f32 v118, v118, s33, 0.5
	v_fma_f32 v119, v119, s33, 0.5
	v_max_u32_e32 v115, 1, v115
	global_store_dwordx2 v[122:123], v[126:127], off
	v_cvt_u32_f32_e32 v118, v118
	v_cvt_u32_f32_e32 v119, v119
	v_fma_f32 v120, v121, s33, 0.5
	v_max_u32_sdwa v121, v114, v228 dst_sel:WORD_1 dst_unused:UNUSED_PAD src0_sel:DWORD src1_sel:DWORD
	v_max_u32_sdwa v126, v116, v228 dst_sel:WORD_1 dst_unused:UNUSED_PAD src0_sel:DWORD src1_sel:DWORD
	v_max_u32_sdwa v117, v117, v228 dst_sel:BYTE_3 dst_unused:UNUSED_PAD src0_sel:DWORD src1_sel:DWORD
	v_add_u32_e32 v114, 16, v124
;     __device__ __forceinline__ void operator()(const AccT& acc, const gm::GUnit& u, int wr, int wc, int fr, int fq) const {
;     ...
;             for (int bj = 0; bj < 2; ++bj) {
;                 const f32x4 b0 = bb[bj][0], b1 = bb[bj][1];
; #pragma unroll
;                 for (int ai = 0; ai < 2; ++ai)
; #pragma unroll
;                     for (int m = 0; m < 4; ++m) {
;                         const int row = u.pm * 256 + ai * 128 + wr * 64 + m * 16 + fr;
;                         f32x4 v0 = (acc[ai][bj][m][0] + b0) * -1.4426950408889634f, v1 = (acc[ai][bj][m][1] + b1) * -1.4426950408889634f;
; #pragma unroll
;                         for (int j = 0; j < 4; ++j) { v0[j] = __builtin_amdgcn_exp2f(v0[j]); v1[j] = __builtin_amdgcn_exp2f(v1[j]); }
;                         v0 = v0 + 1.f; v1 = v1 + 1.f;
; #pragma unroll
;                         for (int j = 0; j < 4; ++j) { v0[j] = __builtin_amdgcn_rcpf(v0[j]); v1[j] = __builtin_amdgcn_rcpf(v1[j]); }
;                         v0 = v0 * 255.f + 0.5f; v1 = v1 * 255.f + 0.5f;
;                         unsigned q[8];
; #pragma unroll
;                         for (int j = 0; j < 4; ++j) { q[j] = max((unsigned)v0[j], 1u); q[4 + j] = max((unsigned)v1[j], 1u); }
;                         u32x2 w; w.x = q[0] | (q[1] << 8) | (q[2] << 16) | (q[3] << 24); w.y = q[4] | (q[5] << 8) | (q[6] << 16) | (q[7] << 24);
;                         *(u32x2*)(G8 + (size_t)row * INW + u.pn * 256 + bj * 128 + wc * 32 + 8 * fq) = w;
;                     }
	v_lshl_or_b32 v115, v115, 8, v125
	v_pk_add_f32 v[110:111], v[110:111], v[142:143]
	v_cvt_u32_f32_e32 v120, v120
	v_or3_b32 v117, v115, v126, v117
	v_ashrrev_i32_e32 v115, 31, v114
	v_pk_mul_f32 v[110:111], v[110:111], s[6:7] op_sel_hi:[1,0]
	v_lshlrev_b64 v[114:115], 12, v[114:115]
	v_exp_f32_e32 v110, v110
	v_exp_f32_e32 v111, v111
	v_pk_add_f32 v[112:113], v[112:113], 1.0 op_sel_hi:[1,0]
	v_pk_add_f32 v[108:109], v[108:109], 1.0 op_sel_hi:[1,0]
	v_rcp_f32_e32 v107, v107
	v_fma_f32 v106, v106, s33, 0.5
	v_lshl_add_u64 v[114:115], s[46:47], 0, v[114:115]
	v_rcp_f32_e32 v112, v112
	v_rcp_f32_e32 v108, v108
	v_rcp_f32_e32 v109, v109
	v_cvt_u32_f32_e32 v106, v106
	v_pk_add_f32 v[98:99], v[98:99], v[138:139]
	v_max_u32_e32 v118, 1, v118
	v_max_u32_e32 v119, 1, v119
	v_lshl_add_u64 v[114:115], v[114:115], 0, s[18:19]
	v_pk_mul_f32 v[98:99], v[98:99], s[6:7] op_sel_hi:[1,0]
	v_max_u32_sdwa v116, v120, v228 dst_sel:BYTE_3 dst_unused:UNUSED_PAD src0_sel:DWORD src1_sel:DWORD
	v_lshl_or_b32 v118, v119, 8, v118
	v_lshl_add_u64 v[114:115], v[114:115], 0, s[48:49]
	v_exp_f32_e32 v98, v98
	v_exp_f32_e32 v99, v99
	v_or3_b32 v116, v118, v121, v116
	v_lshl_add_u64 v[114:115], v[114:115], 0, v[148:149]
	v_pk_add_f32 v[110:111], v[110:111], 1.0 op_sel_hi:[1,0]
	v_fma_f32 v107, v107, s33, 0.5
	global_store_dwordx2 v[114:115], v[116:117], off
	v_rcp_f32_e32 v110, v110
	v_rcp_f32_e32 v111, v111
	v_cvt_u32_f32_e32 v107, v107
	v_max_u32_e32 v116, 1, v106
	v_fma_f32 v106, v112, s33, 0.5
	v_fma_f32 v108, v108, s33, 0.5
	v_fma_f32 v109, v109, s33, 0.5
	v_rcp_f32_e32 v113, v113
	v_cvt_u32_f32_e32 v106, v106
	v_cvt_u32_f32_e32 v108, v108
	v_cvt_u32_f32_e32 v109, v109
	v_pk_add_f32 v[104:105], v[104:105], v[144:145]
	v_pk_add_f32 v[100:101], v[100:101], v[140:141]
	v_pk_mul_f32 v[104:105], v[104:105], s[6:7] op_sel_hi:[1,0]
	v_pk_mul_f32 v[100:101], v[100:101], s[6:7] op_sel_hi:[1,0]
	v_pk_add_f32 v[98:99], v[98:99], 1.0 op_sel_hi:[1,0]
	v_exp_f32_e32 v104, v104
	v_exp_f32_e32 v105, v105
	v_exp_f32_e32 v100, v100
	v_exp_f32_e32 v101, v101
	v_rcp_f32_e32 v98, v98
	v_fma_f32 v110, v110, s33, 0.5
	v_fma_f32 v111, v111, s33, 0.5
	v_max_u32_e32 v107, 1, v107
	v_cvt_u32_f32_e32 v110, v110
	v_cvt_u32_f32_e32 v111, v111
	v_fma_f32 v112, v113, s33, 0.5
	v_max_u32_sdwa v113, v106, v228 dst_sel:WORD_1 dst_unused:UNUSED_PAD src0_sel:DWORD src1_sel:DWORD
	v_max_u32_sdwa v117, v108, v228 dst_sel:WORD_1 dst_unused:UNUSED_PAD src0_sel:DWORD src1_sel:DWORD
	v_max_u32_sdwa v109, v109, v228 dst_sel:BYTE_3 dst_unused:UNUSED_PAD src0_sel:DWORD src1_sel:DWORD
	v_add_u32_e32 v106, 32, v124
	v_lshl_or_b32 v107, v107, 8, v116
	v_pk_add_f32 v[102:103], v[102:103], v[142:143]
	v_cvt_u32_f32_e32 v112, v112
	v_or3_b32 v109, v107, v117, v109
	v_ashrrev_i32_e32 v107, 31, v106
	v_pk_mul_f32 v[102:103], v[102:103], s[6:7] op_sel_hi:[1,0]
	v_lshlrev_b64 v[106:107], 12, v[106:107]
	v_exp_f32_e32 v102, v102
	v_exp_f32_e32 v103, v103
	v_pk_add_f32 v[104:105], v[104:105], 1.0 op_sel_hi:[1,0]
	v_pk_add_f32 v[100:101], v[100:101], 1.0 op_sel_hi:[1,0]
	v_rcp_f32_e32 v99, v99
	v_fma_f32 v98, v98, s33, 0.5
	v_lshl_add_u64 v[106:107], s[46:47], 0, v[106:107]
	v_rcp_f32_e32 v104, v104
	v_rcp_f32_e32 v100, v100
	v_rcp_f32_e32 v101, v101
	v_cvt_u32_f32_e32 v98, v98
	v_pk_add_f32 v[90:91], v[90:91], v[138:139]
	v_max_u32_e32 v110, 1, v110
	v_max_u32_e32 v111, 1, v111
	v_lshl_add_u64 v[106:107], v[106:107], 0, s[18:19]
	v_pk_mul_f32 v[90:91], v[90:91], s[6:7] op_sel_hi:[1,0]
	v_max_u32_sdwa v108, v112, v228 dst_sel:BYTE_3 dst_unused:UNUSED_PAD src0_sel:DWORD src1_sel:DWORD
	v_lshl_or_b32 v110, v111, 8, v110
	v_lshl_add_u64 v[106:107], v[106:107], 0, s[48:49]
	v_exp_f32_e32 v90, v90
	v_exp_f32_e32 v91, v91
	v_or3_b32 v108, v110, v113, v108
	v_lshl_add_u64 v[106:107], v[106:107], 0, v[148:149]
	v_pk_add_f32 v[102:103], v[102:103], 1.0 op_sel_hi:[1,0]
	v_fma_f32 v99, v99, s33, 0.5
	global_store_dwordx2 v[106:107], v[108:109], off
	v_rcp_f32_e32 v102, v102
	v_rcp_f32_e32 v103, v103
	v_cvt_u32_f32_e32 v99, v99
	v_max_u32_e32 v108, 1, v98
	v_fma_f32 v98, v104, s33, 0.5
	v_fma_f32 v100, v100, s33, 0.5
	v_fma_f32 v101, v101, s33, 0.5
	v_rcp_f32_e32 v105, v105
	v_cvt_u32_f32_e32 v98, v98
	v_cvt_u32_f32_e32 v100, v100
	v_cvt_u32_f32_e32 v101, v101
	v_pk_add_f32 v[96:97], v[96:97], v[144:145]
	v_pk_add_f32 v[92:93], v[92:93], v[140:141]
	v_pk_mul_f32 v[96:97], v[96:97], s[6:7] op_sel_hi:[1,0]
	v_pk_mul_f32 v[92:93], v[92:93], s[6:7] op_sel_hi:[1,0]
	v_pk_add_f32 v[90:91], v[90:91], 1.0 op_sel_hi:[1,0]
	v_exp_f32_e32 v96, v96
	v_exp_f32_e32 v97, v97
	v_exp_f32_e32 v92, v92
	v_exp_f32_e32 v93, v93
	v_rcp_f32_e32 v90, v90
	v_fma_f32 v102, v102, s33, 0.5
	v_fma_f32 v103, v103, s33, 0.5
	v_max_u32_e32 v99, 1, v99
	v_cvt_u32_f32_e32 v102, v102
	v_cvt_u32_f32_e32 v103, v103
	v_fma_f32 v104, v105, s33, 0.5
	v_max_u32_sdwa v105, v98, v228 dst_sel:WORD_1 dst_unused:UNUSED_PAD src0_sel:DWORD src1_sel:DWORD
	v_max_u32_sdwa v109, v100, v228 dst_sel:WORD_1 dst_unused:UNUSED_PAD src0_sel:DWORD src1_sel:DWORD
	v_max_u32_sdwa v101, v101, v228 dst_sel:BYTE_3 dst_unused:UNUSED_PAD src0_sel:DWORD src1_sel:DWORD
	v_add_u32_e32 v98, 48, v124
	v_lshl_or_b32 v99, v99, 8, v108
	v_pk_add_f32 v[94:95], v[94:95], v[142:143]
	v_cvt_u32_f32_e32 v104, v104
	v_or3_b32 v101, v99, v109, v101
	v_ashrrev_i32_e32 v99, 31, v98
	v_pk_mul_f32 v[94:95], v[94:95], s[6:7] op_sel_hi:[1,0]
	v_lshlrev_b64 v[98:99], 12, v[98:99]
	v_exp_f32_e32 v94, v94
	v_exp_f32_e32 v95, v95
	v_pk_add_f32 v[96:97], v[96:97], 1.0 op_sel_hi:[1,0]
	v_pk_add_f32 v[92:93], v[92:93], 1.0 op_sel_hi:[1,0]
	v_rcp_f32_e32 v91, v91
	v_fma_f32 v90, v90, s33, 0.5
	v_lshl_add_u64 v[98:99], s[46:47], 0, v[98:99]
;     __device__ __forceinline__ void operator()(const AccT& acc, const gm::GUnit& u, int wr, int wc, int fr, int fq) const {
;     ...
;             for (int bj = 0; bj < 2; ++bj) {
;                 const f32x4 b0 = bb[bj][0], b1 = bb[bj][1];
; #pragma unroll
;                 for (int ai = 0; ai < 2; ++ai)
; #pragma unroll
;                     for (int m = 0; m < 4; ++m) {
;                         const int row = u.pm * 256 + ai * 128 + wr * 64 + m * 16 + fr;
;                         f32x4 v0 = (acc[ai][bj][m][0] + b0) * -1.4426950408889634f, v1 = (acc[ai][bj][m][1] + b1) * -1.4426950408889634f;
; #pragma unroll
;                         for (int j = 0; j < 4; ++j) { v0[j] = __builtin_amdgcn_exp2f(v0[j]); v1[j] = __builtin_amdgcn_exp2f(v1[j]); }
;                         v0 = v0 + 1.f; v1 = v1 + 1.f;
; #pragma unroll
;                         for (int j = 0; j < 4; ++j) { v0[j] = __builtin_amdgcn_rcpf(v0[j]); v1[j] = __builtin_amdgcn_rcpf(v1[j]); }
;                         v0 = v0 * 255.f + 0.5f; v1 = v1 * 255.f + 0.5f;
;                         unsigned q[8];
; #pragma unroll
;                         for (int j = 0; j < 4; ++j) { q[j] = max((unsigned)v0[j], 1u); q[4 + j] = max((unsigned)v1[j], 1u); }
;                         u32x2 w; w.x = q[0] | (q[1] << 8) | (q[2] << 16) | (q[3] << 24); w.y = q[4] | (q[5] << 8) | (q[6] << 16) | (q[7] << 24);
;                         *(u32x2*)(G8 + (size_t)row * INW + u.pn * 256 + bj * 128 + wc * 32 + 8 * fq) = w;
;                     }
	v_rcp_f32_e32 v96, v96
	v_rcp_f32_e32 v92, v92
	v_rcp_f32_e32 v93, v93
	v_cvt_u32_f32_e32 v90, v90
	v_pk_add_f32 v[82:83], v[82:83], v[138:139]
	v_max_u32_e32 v102, 1, v102
	v_max_u32_e32 v103, 1, v103
	v_lshl_add_u64 v[98:99], v[98:99], 0, s[18:19]
	v_pk_mul_f32 v[82:83], v[82:83], s[6:7] op_sel_hi:[1,0]
	v_max_u32_sdwa v100, v104, v228 dst_sel:BYTE_3 dst_unused:UNUSED_PAD src0_sel:DWORD src1_sel:DWORD
	v_lshl_or_b32 v102, v103, 8, v102
	v_lshl_add_u64 v[98:99], v[98:99], 0, s[48:49]
	v_exp_f32_e32 v82, v82
	v_exp_f32_e32 v83, v83
	v_or3_b32 v100, v102, v105, v100
	v_lshl_add_u64 v[98:99], v[98:99], 0, v[148:149]
	v_pk_add_f32 v[94:95], v[94:95], 1.0 op_sel_hi:[1,0]
	v_fma_f32 v91, v91, s33, 0.5
	global_store_dwordx2 v[98:99], v[100:101], off
	v_rcp_f32_e32 v94, v94
	v_rcp_f32_e32 v95, v95
	v_cvt_u32_f32_e32 v91, v91
	v_max_u32_e32 v100, 1, v90
	v_fma_f32 v90, v96, s33, 0.5
	v_fma_f32 v92, v92, s33, 0.5
	v_fma_f32 v93, v93, s33, 0.5
	v_rcp_f32_e32 v97, v97
	v_cvt_u32_f32_e32 v90, v90
	v_cvt_u32_f32_e32 v92, v92
	v_cvt_u32_f32_e32 v93, v93
	v_pk_add_f32 v[88:89], v[88:89], v[144:145]
	v_pk_add_f32 v[84:85], v[84:85], v[140:141]
	v_pk_mul_f32 v[88:89], v[88:89], s[6:7] op_sel_hi:[1,0]
	v_pk_mul_f32 v[84:85], v[84:85], s[6:7] op_sel_hi:[1,0]
	v_pk_add_f32 v[82:83], v[82:83], 1.0 op_sel_hi:[1,0]
	v_exp_f32_e32 v88, v88
	v_exp_f32_e32 v89, v89
	v_exp_f32_e32 v84, v84
	v_exp_f32_e32 v85, v85
	v_rcp_f32_e32 v82, v82
	v_fma_f32 v94, v94, s33, 0.5
	v_fma_f32 v95, v95, s33, 0.5
	v_max_u32_e32 v91, 1, v91
	v_cvt_u32_f32_e32 v94, v94
	v_cvt_u32_f32_e32 v95, v95
	v_fma_f32 v96, v97, s33, 0.5
	v_max_u32_sdwa v97, v90, v228 dst_sel:WORD_1 dst_unused:UNUSED_PAD src0_sel:DWORD src1_sel:DWORD
	v_max_u32_sdwa v101, v92, v228 dst_sel:WORD_1 dst_unused:UNUSED_PAD src0_sel:DWORD src1_sel:DWORD
	v_max_u32_sdwa v93, v93, v228 dst_sel:BYTE_3 dst_unused:UNUSED_PAD src0_sel:DWORD src1_sel:DWORD
	v_add_u32_e32 v90, 0x80, v124
	v_lshl_or_b32 v91, v91, 8, v100
	v_pk_add_f32 v[86:87], v[86:87], v[142:143]
	v_cvt_u32_f32_e32 v96, v96
	v_or3_b32 v93, v91, v101, v93
	v_ashrrev_i32_e32 v91, 31, v90
	v_pk_mul_f32 v[86:87], v[86:87], s[6:7] op_sel_hi:[1,0]
	v_lshlrev_b64 v[90:91], 12, v[90:91]
	v_exp_f32_e32 v86, v86
	v_exp_f32_e32 v87, v87
	v_pk_add_f32 v[88:89], v[88:89], 1.0 op_sel_hi:[1,0]
	v_pk_add_f32 v[84:85], v[84:85], 1.0 op_sel_hi:[1,0]
	v_rcp_f32_e32 v83, v83
	v_fma_f32 v82, v82, s33, 0.5
	v_lshl_add_u64 v[90:91], s[46:47], 0, v[90:91]
	v_rcp_f32_e32 v88, v88
	v_rcp_f32_e32 v84, v84
	v_rcp_f32_e32 v85, v85
	v_cvt_u32_f32_e32 v82, v82
	v_pk_add_f32 v[74:75], v[74:75], v[138:139]
	v_max_u32_e32 v94, 1, v94
	v_max_u32_e32 v95, 1, v95
	v_lshl_add_u64 v[90:91], v[90:91], 0, s[18:19]
	v_pk_mul_f32 v[74:75], v[74:75], s[6:7] op_sel_hi:[1,0]
	v_max_u32_sdwa v92, v96, v228 dst_sel:BYTE_3 dst_unused:UNUSED_PAD src0_sel:DWORD src1_sel:DWORD
	v_lshl_or_b32 v94, v95, 8, v94
	v_lshl_add_u64 v[90:91], v[90:91], 0, s[48:49]
	v_exp_f32_e32 v74, v74
	v_exp_f32_e32 v75, v75
	v_or3_b32 v92, v94, v97, v92
	v_lshl_add_u64 v[90:91], v[90:91], 0, v[148:149]
	v_pk_add_f32 v[86:87], v[86:87], 1.0 op_sel_hi:[1,0]
	v_fma_f32 v83, v83, s33, 0.5
	global_store_dwordx2 v[90:91], v[92:93], off
	v_rcp_f32_e32 v86, v86
	v_rcp_f32_e32 v87, v87
	v_cvt_u32_f32_e32 v83, v83
	v_max_u32_e32 v92, 1, v82
	v_fma_f32 v82, v88, s33, 0.5
	v_fma_f32 v84, v84, s33, 0.5
	v_fma_f32 v85, v85, s33, 0.5
	v_rcp_f32_e32 v89, v89
	v_cvt_u32_f32_e32 v82, v82
	v_cvt_u32_f32_e32 v84, v84
	v_cvt_u32_f32_e32 v85, v85
	v_pk_add_f32 v[80:81], v[80:81], v[144:145]
	v_pk_add_f32 v[76:77], v[76:77], v[140:141]
	v_pk_mul_f32 v[80:81], v[80:81], s[6:7] op_sel_hi:[1,0]
	v_pk_mul_f32 v[76:77], v[76:77], s[6:7] op_sel_hi:[1,0]
	v_pk_add_f32 v[74:75], v[74:75], 1.0 op_sel_hi:[1,0]
	v_exp_f32_e32 v80, v80
	v_exp_f32_e32 v81, v81
	v_exp_f32_e32 v76, v76
	v_exp_f32_e32 v77, v77
	v_rcp_f32_e32 v74, v74
	v_fma_f32 v86, v86, s33, 0.5
	v_fma_f32 v87, v87, s33, 0.5
	v_max_u32_e32 v83, 1, v83
	v_cvt_u32_f32_e32 v86, v86
	v_cvt_u32_f32_e32 v87, v87
	v_fma_f32 v88, v89, s33, 0.5
	v_max_u32_sdwa v89, v82, v228 dst_sel:WORD_1 dst_unused:UNUSED_PAD src0_sel:DWORD src1_sel:DWORD
	v_max_u32_sdwa v93, v84, v228 dst_sel:WORD_1 dst_unused:UNUSED_PAD src0_sel:DWORD src1_sel:DWORD
	v_max_u32_sdwa v85, v85, v228 dst_sel:BYTE_3 dst_unused:UNUSED_PAD src0_sel:DWORD src1_sel:DWORD
	v_add_u32_e32 v82, 0x90, v124
	v_lshl_or_b32 v83, v83, 8, v92
	v_pk_add_f32 v[78:79], v[78:79], v[142:143]
	v_cvt_u32_f32_e32 v88, v88
	v_or3_b32 v85, v83, v93, v85
	v_ashrrev_i32_e32 v83, 31, v82
	v_pk_mul_f32 v[78:79], v[78:79], s[6:7] op_sel_hi:[1,0]
	v_lshlrev_b64 v[82:83], 12, v[82:83]
	v_exp_f32_e32 v78, v78
	v_exp_f32_e32 v79, v79
	v_pk_add_f32 v[80:81], v[80:81], 1.0 op_sel_hi:[1,0]
	v_pk_add_f32 v[76:77], v[76:77], 1.0 op_sel_hi:[1,0]
	v_rcp_f32_e32 v75, v75
	v_fma_f32 v74, v74, s33, 0.5
	v_lshl_add_u64 v[82:83], s[46:47], 0, v[82:83]
	v_rcp_f32_e32 v80, v80
	v_rcp_f32_e32 v76, v76
	v_rcp_f32_e32 v77, v77
	v_cvt_u32_f32_e32 v74, v74
	v_pk_add_f32 v[66:67], v[66:67], v[138:139]
	v_max_u32_e32 v86, 1, v86
	v_max_u32_e32 v87, 1, v87
	v_lshl_add_u64 v[82:83], v[82:83], 0, s[18:19]
	v_pk_mul_f32 v[66:67], v[66:67], s[6:7] op_sel_hi:[1,0]
	v_max_u32_sdwa v84, v88, v228 dst_sel:BYTE_3 dst_unused:UNUSED_PAD src0_sel:DWORD src1_sel:DWORD
	v_lshl_or_b32 v86, v87, 8, v86
	v_lshl_add_u64 v[82:83], v[82:83], 0, s[48:49]
	v_exp_f32_e32 v66, v66
	v_exp_f32_e32 v67, v67
	v_or3_b32 v84, v86, v89, v84
	v_lshl_add_u64 v[82:83], v[82:83], 0, v[148:149]
	v_pk_add_f32 v[78:79], v[78:79], 1.0 op_sel_hi:[1,0]
	v_fma_f32 v75, v75, s33, 0.5
	global_store_dwordx2 v[82:83], v[84:85], off
;     __device__ __forceinline__ void operator()(const AccT& acc, const gm::GUnit& u, int wr, int wc, int fr, int fq) const {
;     ...
;             for (int bj = 0; bj < 2; ++bj) {
;                 const f32x4 b0 = bb[bj][0], b1 = bb[bj][1];
; #pragma unroll
;                 for (int ai = 0; ai < 2; ++ai)
; #pragma unroll
;                     for (int m = 0; m < 4; ++m) {
;                         const int row = u.pm * 256 + ai * 128 + wr * 64 + m * 16 + fr;
;                         f32x4 v0 = (acc[ai][bj][m][0] + b0) * -1.4426950408889634f, v1 = (acc[ai][bj][m][1] + b1) * -1.4426950408889634f;
; #pragma unroll
;                         for (int j = 0; j < 4; ++j) { v0[j] = __builtin_amdgcn_exp2f(v0[j]); v1[j] = __builtin_amdgcn_exp2f(v1[j]); }
;                         v0 = v0 + 1.f; v1 = v1 + 1.f;
; #pragma unroll
;                         for (int j = 0; j < 4; ++j) { v0[j] = __builtin_amdgcn_rcpf(v0[j]); v1[j] = __builtin_amdgcn_rcpf(v1[j]); }
;                         v0 = v0 * 255.f + 0.5f; v1 = v1 * 255.f + 0.5f;
;                         unsigned q[8];
; #pragma unroll
;                         for (int j = 0; j < 4; ++j) { q[j] = max((unsigned)v0[j], 1u); q[4 + j] = max((unsigned)v1[j], 1u); }
;                         u32x2 w; w.x = q[0] | (q[1] << 8) | (q[2] << 16) | (q[3] << 24); w.y = q[4] | (q[5] << 8) | (q[6] << 16) | (q[7] << 24);
;                         *(u32x2*)(G8 + (size_t)row * INW + u.pn * 256 + bj * 128 + wc * 32 + 8 * fq) = w;
;                     }
	v_rcp_f32_e32 v78, v78
	v_rcp_f32_e32 v79, v79
	v_cvt_u32_f32_e32 v75, v75
	v_max_u32_e32 v84, 1, v74
	v_fma_f32 v74, v80, s33, 0.5
	v_fma_f32 v76, v76, s33, 0.5
	v_fma_f32 v77, v77, s33, 0.5
	v_rcp_f32_e32 v81, v81
	v_cvt_u32_f32_e32 v74, v74
	v_cvt_u32_f32_e32 v76, v76
	v_cvt_u32_f32_e32 v77, v77
	v_pk_add_f32 v[72:73], v[72:73], v[144:145]
	v_pk_add_f32 v[68:69], v[68:69], v[140:141]
	v_pk_mul_f32 v[72:73], v[72:73], s[6:7] op_sel_hi:[1,0]
	v_pk_mul_f32 v[68:69], v[68:69], s[6:7] op_sel_hi:[1,0]
	v_pk_add_f32 v[66:67], v[66:67], 1.0 op_sel_hi:[1,0]
	v_exp_f32_e32 v72, v72
	v_exp_f32_e32 v73, v73
	v_exp_f32_e32 v68, v68
	v_exp_f32_e32 v69, v69
	v_rcp_f32_e32 v66, v66
	v_fma_f32 v78, v78, s33, 0.5
	v_fma_f32 v79, v79, s33, 0.5
	v_max_u32_e32 v75, 1, v75
	v_cvt_u32_f32_e32 v78, v78
	v_cvt_u32_f32_e32 v79, v79
	v_fma_f32 v80, v81, s33, 0.5
	v_max_u32_sdwa v81, v74, v228 dst_sel:WORD_1 dst_unused:UNUSED_PAD src0_sel:DWORD src1_sel:DWORD
	v_max_u32_sdwa v85, v76, v228 dst_sel:WORD_1 dst_unused:UNUSED_PAD src0_sel:DWORD src1_sel:DWORD
	v_max_u32_sdwa v77, v77, v228 dst_sel:BYTE_3 dst_unused:UNUSED_PAD src0_sel:DWORD src1_sel:DWORD
	v_add_u32_e32 v74, 0xa0, v124
	v_lshl_or_b32 v75, v75, 8, v84
	v_pk_add_f32 v[70:71], v[70:71], v[142:143]
	v_cvt_u32_f32_e32 v80, v80
	v_or3_b32 v77, v75, v85, v77
	v_ashrrev_i32_e32 v75, 31, v74
	v_pk_mul_f32 v[70:71], v[70:71], s[6:7] op_sel_hi:[1,0]
	v_lshlrev_b64 v[74:75], 12, v[74:75]
	v_exp_f32_e32 v70, v70
	v_exp_f32_e32 v71, v71
	v_pk_add_f32 v[72:73], v[72:73], 1.0 op_sel_hi:[1,0]
	v_pk_add_f32 v[68:69], v[68:69], 1.0 op_sel_hi:[1,0]
	v_rcp_f32_e32 v67, v67
	v_fma_f32 v66, v66, s33, 0.5
	v_lshl_add_u64 v[74:75], s[46:47], 0, v[74:75]
	v_rcp_f32_e32 v72, v72
	v_rcp_f32_e32 v68, v68
	v_rcp_f32_e32 v69, v69
	v_cvt_u32_f32_e32 v66, v66
	v_pk_add_f32 v[62:63], v[62:63], v[134:135]
	v_pk_add_f32 v[58:59], v[58:59], v[130:131]
	v_max_u32_e32 v78, 1, v78
	v_max_u32_e32 v79, 1, v79
	v_lshl_add_u64 v[74:75], v[74:75], 0, s[18:19]
	v_pk_mul_f32 v[62:63], v[62:63], s[6:7] op_sel_hi:[1,0]
	v_pk_mul_f32 v[58:59], v[58:59], s[6:7] op_sel_hi:[1,0]
	v_max_u32_sdwa v76, v80, v228 dst_sel:BYTE_3 dst_unused:UNUSED_PAD src0_sel:DWORD src1_sel:DWORD
	v_lshl_or_b32 v78, v79, 8, v78
	v_lshl_add_u64 v[74:75], v[74:75], 0, s[48:49]
	v_exp_f32_e32 v62, v62
	v_exp_f32_e32 v58, v58
	v_exp_f32_e32 v63, v63
	v_exp_f32_e32 v59, v59
	v_or3_b32 v76, v78, v81, v76
	v_lshl_add_u64 v[74:75], v[74:75], 0, v[148:149]
	v_pk_add_f32 v[70:71], v[70:71], 1.0 op_sel_hi:[1,0]
	v_fma_f32 v67, v67, s33, 0.5
	global_store_dwordx2 v[74:75], v[76:77], off
	v_rcp_f32_e32 v70, v70
	v_rcp_f32_e32 v71, v71
	v_cvt_u32_f32_e32 v67, v67
	v_max_u32_e32 v76, 1, v66
	v_fma_f32 v66, v72, s33, 0.5
	v_fma_f32 v68, v68, s33, 0.5
	v_fma_f32 v69, v69, s33, 0.5
	v_rcp_f32_e32 v73, v73
	v_cvt_u32_f32_e32 v66, v66
	v_cvt_u32_f32_e32 v68, v68
	v_cvt_u32_f32_e32 v69, v69
	v_pk_add_f32 v[64:65], v[64:65], v[136:137]
	v_pk_add_f32 v[60:61], v[60:61], v[132:133]
	v_pk_mul_f32 v[64:65], v[64:65], s[6:7] op_sel_hi:[1,0]
	v_pk_mul_f32 v[60:61], v[60:61], s[6:7] op_sel_hi:[1,0]
	v_pk_add_f32 v[62:63], v[62:63], 1.0 op_sel_hi:[1,0]
	v_pk_add_f32 v[58:59], v[58:59], 1.0 op_sel_hi:[1,0]
	v_exp_f32_e32 v64, v64
	v_exp_f32_e32 v65, v65
	v_exp_f32_e32 v60, v60
	v_exp_f32_e32 v61, v61
	v_rcp_f32_e32 v58, v58
	v_rcp_f32_e32 v63, v63
	v_pk_add_f32 v[54:55], v[54:55], v[134:135]
	v_pk_add_f32 v[50:51], v[50:51], v[130:131]
	v_fma_f32 v70, v70, s33, 0.5
	v_fma_f32 v71, v71, s33, 0.5
	v_max_u32_e32 v67, 1, v67
	v_pk_mul_f32 v[54:55], v[54:55], s[6:7] op_sel_hi:[1,0]
	v_pk_mul_f32 v[50:51], v[50:51], s[6:7] op_sel_hi:[1,0]
	v_cvt_u32_f32_e32 v70, v70
	v_cvt_u32_f32_e32 v71, v71
	v_fma_f32 v72, v73, s33, 0.5
	v_max_u32_sdwa v73, v66, v228 dst_sel:WORD_1 dst_unused:UNUSED_PAD src0_sel:DWORD src1_sel:DWORD
	v_max_u32_sdwa v77, v68, v228 dst_sel:WORD_1 dst_unused:UNUSED_PAD src0_sel:DWORD src1_sel:DWORD
	v_max_u32_sdwa v69, v69, v228 dst_sel:BYTE_3 dst_unused:UNUSED_PAD src0_sel:DWORD src1_sel:DWORD
	v_add_u32_e32 v66, 0xb0, v124
	v_lshl_or_b32 v67, v67, 8, v76
	v_exp_f32_e32 v54, v54
	v_exp_f32_e32 v50, v50
	v_exp_f32_e32 v55, v55
	v_exp_f32_e32 v51, v51
	v_cvt_u32_f32_e32 v72, v72
	v_or3_b32 v69, v67, v77, v69
	v_ashrrev_i32_e32 v67, 31, v66
	v_lshlrev_b64 v[66:67], 12, v[66:67]
	v_pk_add_f32 v[64:65], v[64:65], 1.0 op_sel_hi:[1,0]
	v_pk_add_f32 v[60:61], v[60:61], 1.0 op_sel_hi:[1,0]
	v_rcp_f32_e32 v62, v62
	v_rcp_f32_e32 v59, v59
	v_fma_f32 v58, v58, s33, 0.5
	v_fma_f32 v63, v63, s33, 0.5
	v_lshl_add_u64 v[66:67], s[46:47], 0, v[66:67]
	v_rcp_f32_e32 v64, v64
	v_rcp_f32_e32 v60, v60
	v_rcp_f32_e32 v65, v65
	v_rcp_f32_e32 v61, v61
	v_cvt_u32_f32_e32 v58, v58
	v_cvt_u32_f32_e32 v63, v63
	v_pk_add_f32 v[56:57], v[56:57], v[136:137]
	v_pk_add_f32 v[52:53], v[52:53], v[132:133]
	v_max_u32_e32 v70, 1, v70
	v_max_u32_e32 v71, 1, v71
	v_lshl_add_u64 v[66:67], v[66:67], 0, s[18:19]
	v_pk_mul_f32 v[56:57], v[56:57], s[6:7] op_sel_hi:[1,0]
	v_pk_mul_f32 v[52:53], v[52:53], s[6:7] op_sel_hi:[1,0]
	v_pk_add_f32 v[54:55], v[54:55], 1.0 op_sel_hi:[1,0]
	v_pk_add_f32 v[50:51], v[50:51], 1.0 op_sel_hi:[1,0]
	v_max_u32_sdwa v68, v72, v228 dst_sel:BYTE_3 dst_unused:UNUSED_PAD src0_sel:DWORD src1_sel:DWORD
	v_lshl_or_b32 v70, v71, 8, v70
	v_lshl_add_u64 v[66:67], v[66:67], 0, s[48:49]
	v_exp_f32_e32 v56, v56
	v_exp_f32_e32 v57, v57
	v_exp_f32_e32 v52, v52
	v_exp_f32_e32 v53, v53
	v_rcp_f32_e32 v50, v50
	v_rcp_f32_e32 v55, v55
	v_pk_add_f32 v[46:47], v[46:47], v[134:135]
	v_pk_add_f32 v[42:43], v[42:43], v[130:131]
	v_or3_b32 v68, v70, v73, v68
	v_lshl_add_u64 v[66:67], v[66:67], 0, v[148:149]
	v_fma_f32 v62, v62, s33, 0.5
;     __device__ __forceinline__ void operator()(const AccT& acc, const gm::GUnit& u, int wr, int wc, int fr, int fq) const {
;     ...
;             for (int bj = 0; bj < 2; ++bj) {
;                 const f32x4 b0 = bb[bj][0], b1 = bb[bj][1];
; #pragma unroll
;                 for (int ai = 0; ai < 2; ++ai)
; #pragma unroll
;                     for (int m = 0; m < 4; ++m) {
;                         const int row = u.pm * 256 + ai * 128 + wr * 64 + m * 16 + fr;
;                         f32x4 v0 = (acc[ai][bj][m][0] + b0) * -1.4426950408889634f, v1 = (acc[ai][bj][m][1] + b1) * -1.4426950408889634f;
; #pragma unroll
;                         for (int j = 0; j < 4; ++j) { v0[j] = __builtin_amdgcn_exp2f(v0[j]); v1[j] = __builtin_amdgcn_exp2f(v1[j]); }
;                         v0 = v0 + 1.f; v1 = v1 + 1.f;
; #pragma unroll
;                         for (int j = 0; j < 4; ++j) { v0[j] = __builtin_amdgcn_rcpf(v0[j]); v1[j] = __builtin_amdgcn_rcpf(v1[j]); }
;                         v0 = v0 * 255.f + 0.5f; v1 = v1 * 255.f + 0.5f;
;                         unsigned q[8];
; #pragma unroll
;                         for (int j = 0; j < 4; ++j) { q[j] = max((unsigned)v0[j], 1u); q[4 + j] = max((unsigned)v1[j], 1u); }
;                         u32x2 w; w.x = q[0] | (q[1] << 8) | (q[2] << 16) | (q[3] << 24); w.y = q[4] | (q[5] << 8) | (q[6] << 16) | (q[7] << 24);
;                         *(u32x2*)(G8 + (size_t)row * INW + u.pn * 256 + bj * 128 + wc * 32 + 8 * fq) = w;
;                     }
	v_fma_f32 v59, v59, s33, 0.5
	v_pk_mul_f32 v[46:47], v[46:47], s[6:7] op_sel_hi:[1,0]
	v_pk_mul_f32 v[42:43], v[42:43], s[6:7] op_sel_hi:[1,0]
	global_store_dwordx2 v[66:67], v[68:69], off
	v_cvt_u32_f32_e32 v62, v62
	v_cvt_u32_f32_e32 v59, v59
	v_max_u32_e32 v68, 1, v58
	v_max_u32_e32 v58, 1, v63
	v_fma_f32 v63, v64, s33, 0.5
	v_fma_f32 v60, v60, s33, 0.5
	v_fma_f32 v64, v65, s33, 0.5
	v_fma_f32 v61, v61, s33, 0.5
	v_exp_f32_e32 v46, v46
	v_exp_f32_e32 v42, v42
	v_exp_f32_e32 v47, v47
	v_exp_f32_e32 v43, v43
	v_cvt_u32_f32_e32 v63, v63
	v_cvt_u32_f32_e32 v60, v60
	v_cvt_u32_f32_e32 v64, v64
	v_cvt_u32_f32_e32 v61, v61
	v_pk_add_f32 v[56:57], v[56:57], 1.0 op_sel_hi:[1,0]
	v_pk_add_f32 v[52:53], v[52:53], 1.0 op_sel_hi:[1,0]
	v_rcp_f32_e32 v54, v54
	v_rcp_f32_e32 v51, v51
	v_fma_f32 v50, v50, s33, 0.5
	v_fma_f32 v55, v55, s33, 0.5
	v_rcp_f32_e32 v56, v56
	v_rcp_f32_e32 v52, v52
	v_rcp_f32_e32 v57, v57
	v_rcp_f32_e32 v53, v53
	v_cvt_u32_f32_e32 v50, v50
	v_cvt_u32_f32_e32 v55, v55
	v_pk_add_f32 v[48:49], v[48:49], v[136:137]
	v_pk_add_f32 v[44:45], v[44:45], v[132:133]
	v_max_u32_e32 v62, 1, v62
	v_max_u32_e32 v59, 1, v59
	v_pk_mul_f32 v[48:49], v[48:49], s[6:7] op_sel_hi:[1,0]
	v_pk_mul_f32 v[44:45], v[44:45], s[6:7] op_sel_hi:[1,0]
	v_pk_add_f32 v[46:47], v[46:47], 1.0 op_sel_hi:[1,0]
	v_pk_add_f32 v[42:43], v[42:43], 1.0 op_sel_hi:[1,0]
	v_max_u32_sdwa v63, v63, v228 dst_sel:WORD_1 dst_unused:UNUSED_PAD src0_sel:DWORD src1_sel:DWORD
	v_max_u32_sdwa v60, v60, v228 dst_sel:WORD_1 dst_unused:UNUSED_PAD src0_sel:DWORD src1_sel:DWORD
	v_max_u32_sdwa v64, v64, v228 dst_sel:BYTE_3 dst_unused:UNUSED_PAD src0_sel:DWORD src1_sel:DWORD
	v_max_u32_sdwa v61, v61, v228 dst_sel:BYTE_3 dst_unused:UNUSED_PAD src0_sel:DWORD src1_sel:DWORD
	v_lshl_or_b32 v58, v58, 8, v62
	v_lshl_or_b32 v59, v59, 8, v68
	v_exp_f32_e32 v48, v48
	v_exp_f32_e32 v49, v49
	v_exp_f32_e32 v44, v44
	v_exp_f32_e32 v45, v45
	v_rcp_f32_e32 v42, v42
	v_rcp_f32_e32 v47, v47
	v_pk_add_f32 v[38:39], v[38:39], v[134:135]
	v_pk_add_f32 v[34:35], v[34:35], v[130:131]
	v_or3_b32 v58, v58, v63, v64
	v_or3_b32 v59, v59, v60, v61
	v_fma_f32 v54, v54, s33, 0.5
	v_fma_f32 v51, v51, s33, 0.5
	v_pk_mul_f32 v[38:39], v[38:39], s[6:7] op_sel_hi:[1,0]
	v_pk_mul_f32 v[34:35], v[34:35], s[6:7] op_sel_hi:[1,0]
	global_store_dwordx2 v[122:123], v[58:59], off offset:128
	v_cvt_u32_f32_e32 v54, v54
	v_cvt_u32_f32_e32 v51, v51
	v_max_u32_e32 v58, 1, v50
	v_max_u32_e32 v50, 1, v55
	v_fma_f32 v55, v56, s33, 0.5
	v_fma_f32 v52, v52, s33, 0.5
	v_fma_f32 v56, v57, s33, 0.5
	v_fma_f32 v53, v53, s33, 0.5
	v_exp_f32_e32 v38, v38
	v_exp_f32_e32 v34, v34
	v_exp_f32_e32 v39, v39
	v_exp_f32_e32 v35, v35
	v_cvt_u32_f32_e32 v55, v55
	v_cvt_u32_f32_e32 v52, v52
	v_cvt_u32_f32_e32 v56, v56
	v_cvt_u32_f32_e32 v53, v53
	v_pk_add_f32 v[48:49], v[48:49], 1.0 op_sel_hi:[1,0]
	v_pk_add_f32 v[44:45], v[44:45], 1.0 op_sel_hi:[1,0]
	v_rcp_f32_e32 v46, v46
	v_rcp_f32_e32 v43, v43
	v_fma_f32 v42, v42, s33, 0.5
	v_fma_f32 v47, v47, s33, 0.5
	v_rcp_f32_e32 v48, v48
	v_rcp_f32_e32 v44, v44
	v_rcp_f32_e32 v49, v49
	v_rcp_f32_e32 v45, v45
	v_cvt_u32_f32_e32 v42, v42
	v_cvt_u32_f32_e32 v47, v47
	v_pk_add_f32 v[40:41], v[40:41], v[136:137]
	v_pk_add_f32 v[36:37], v[36:37], v[132:133]
	v_max_u32_e32 v54, 1, v54
	v_max_u32_e32 v51, 1, v51
	v_pk_mul_f32 v[40:41], v[40:41], s[6:7] op_sel_hi:[1,0]
	v_pk_mul_f32 v[36:37], v[36:37], s[6:7] op_sel_hi:[1,0]
	v_pk_add_f32 v[38:39], v[38:39], 1.0 op_sel_hi:[1,0]
	v_pk_add_f32 v[34:35], v[34:35], 1.0 op_sel_hi:[1,0]
	v_max_u32_sdwa v55, v55, v228 dst_sel:WORD_1 dst_unused:UNUSED_PAD src0_sel:DWORD src1_sel:DWORD
	v_max_u32_sdwa v52, v52, v228 dst_sel:WORD_1 dst_unused:UNUSED_PAD src0_sel:DWORD src1_sel:DWORD
	v_max_u32_sdwa v56, v56, v228 dst_sel:BYTE_3 dst_unused:UNUSED_PAD src0_sel:DWORD src1_sel:DWORD
	v_max_u32_sdwa v53, v53, v228 dst_sel:BYTE_3 dst_unused:UNUSED_PAD src0_sel:DWORD src1_sel:DWORD
	v_lshl_or_b32 v50, v50, 8, v54
	v_lshl_or_b32 v51, v51, 8, v58
	v_exp_f32_e32 v40, v40
	v_exp_f32_e32 v41, v41
	v_exp_f32_e32 v36, v36
	v_exp_f32_e32 v37, v37
	v_rcp_f32_e32 v34, v34
	v_rcp_f32_e32 v39, v39
	v_pk_add_f32 v[30:31], v[30:31], v[134:135]
	v_pk_add_f32 v[26:27], v[26:27], v[130:131]
	v_or3_b32 v50, v50, v55, v56
	v_or3_b32 v51, v51, v52, v53
	v_fma_f32 v46, v46, s33, 0.5
	v_fma_f32 v43, v43, s33, 0.5
	v_pk_mul_f32 v[30:31], v[30:31], s[6:7] op_sel_hi:[1,0]
	v_pk_mul_f32 v[26:27], v[26:27], s[6:7] op_sel_hi:[1,0]
	global_store_dwordx2 v[114:115], v[50:51], off offset:128
	v_cvt_u32_f32_e32 v46, v46
	v_cvt_u32_f32_e32 v43, v43
	v_max_u32_e32 v50, 1, v42
	v_max_u32_e32 v42, 1, v47
	v_fma_f32 v47, v48, s33, 0.5
	v_fma_f32 v44, v44, s33, 0.5
	v_fma_f32 v48, v49, s33, 0.5
	v_fma_f32 v45, v45, s33, 0.5
	v_exp_f32_e32 v30, v30
	v_exp_f32_e32 v26, v26
	v_exp_f32_e32 v31, v31
	v_exp_f32_e32 v27, v27
	v_cvt_u32_f32_e32 v47, v47
	v_cvt_u32_f32_e32 v44, v44
	v_cvt_u32_f32_e32 v48, v48
	v_cvt_u32_f32_e32 v45, v45
	v_pk_add_f32 v[40:41], v[40:41], 1.0 op_sel_hi:[1,0]
	v_pk_add_f32 v[36:37], v[36:37], 1.0 op_sel_hi:[1,0]
	v_rcp_f32_e32 v38, v38
	v_rcp_f32_e32 v35, v35
	v_fma_f32 v34, v34, s33, 0.5
	v_fma_f32 v39, v39, s33, 0.5
	v_rcp_f32_e32 v40, v40
	v_rcp_f32_e32 v36, v36
	v_rcp_f32_e32 v41, v41
	v_rcp_f32_e32 v37, v37
	v_cvt_u32_f32_e32 v34, v34
	v_cvt_u32_f32_e32 v39, v39
	v_pk_add_f32 v[32:33], v[32:33], v[136:137]
	v_pk_add_f32 v[28:29], v[28:29], v[132:133]
	v_max_u32_e32 v46, 1, v46
	v_max_u32_e32 v43, 1, v43
	v_pk_mul_f32 v[32:33], v[32:33], s[6:7] op_sel_hi:[1,0]
	v_pk_mul_f32 v[28:29], v[28:29], s[6:7] op_sel_hi:[1,0]
	v_pk_add_f32 v[30:31], v[30:31], 1.0 op_sel_hi:[1,0]
;     __device__ __forceinline__ void operator()(const AccT& acc, const gm::GUnit& u, int wr, int wc, int fr, int fq) const {
;     ...
;             for (int bj = 0; bj < 2; ++bj) {
;                 const f32x4 b0 = bb[bj][0], b1 = bb[bj][1];
; #pragma unroll
;                 for (int ai = 0; ai < 2; ++ai)
; #pragma unroll
;                     for (int m = 0; m < 4; ++m) {
;                         const int row = u.pm * 256 + ai * 128 + wr * 64 + m * 16 + fr;
;                         f32x4 v0 = (acc[ai][bj][m][0] + b0) * -1.4426950408889634f, v1 = (acc[ai][bj][m][1] + b1) * -1.4426950408889634f;
; #pragma unroll
;                         for (int j = 0; j < 4; ++j) { v0[j] = __builtin_amdgcn_exp2f(v0[j]); v1[j] = __builtin_amdgcn_exp2f(v1[j]); }
;                         v0 = v0 + 1.f; v1 = v1 + 1.f;
; #pragma unroll
;                         for (int j = 0; j < 4; ++j) { v0[j] = __builtin_amdgcn_rcpf(v0[j]); v1[j] = __builtin_amdgcn_rcpf(v1[j]); }
;                         v0 = v0 * 255.f + 0.5f; v1 = v1 * 255.f + 0.5f;
;                         unsigned q[8];
; #pragma unroll
;                         for (int j = 0; j < 4; ++j) { q[j] = max((unsigned)v0[j], 1u); q[4 + j] = max((unsigned)v1[j], 1u); }
;                         u32x2 w; w.x = q[0] | (q[1] << 8) | (q[2] << 16) | (q[3] << 24); w.y = q[4] | (q[5] << 8) | (q[6] << 16) | (q[7] << 24);
;                         *(u32x2*)(G8 + (size_t)row * INW + u.pn * 256 + bj * 128 + wc * 32 + 8 * fq) = w;
;                     }
	v_pk_add_f32 v[26:27], v[26:27], 1.0 op_sel_hi:[1,0]
	v_max_u32_sdwa v47, v47, v228 dst_sel:WORD_1 dst_unused:UNUSED_PAD src0_sel:DWORD src1_sel:DWORD
	v_max_u32_sdwa v44, v44, v228 dst_sel:WORD_1 dst_unused:UNUSED_PAD src0_sel:DWORD src1_sel:DWORD
	v_max_u32_sdwa v48, v48, v228 dst_sel:BYTE_3 dst_unused:UNUSED_PAD src0_sel:DWORD src1_sel:DWORD
	v_max_u32_sdwa v45, v45, v228 dst_sel:BYTE_3 dst_unused:UNUSED_PAD src0_sel:DWORD src1_sel:DWORD
	v_lshl_or_b32 v42, v42, 8, v46
	v_lshl_or_b32 v43, v43, 8, v50
	v_exp_f32_e32 v32, v32
	v_exp_f32_e32 v33, v33
	v_exp_f32_e32 v28, v28
	v_exp_f32_e32 v29, v29
	v_rcp_f32_e32 v26, v26
	v_rcp_f32_e32 v31, v31
	v_pk_add_f32 v[22:23], v[22:23], v[134:135]
	v_pk_add_f32 v[18:19], v[18:19], v[130:131]
	v_or3_b32 v42, v42, v47, v48
	v_or3_b32 v43, v43, v44, v45
	v_fma_f32 v38, v38, s33, 0.5
	v_fma_f32 v35, v35, s33, 0.5
	v_pk_mul_f32 v[22:23], v[22:23], s[6:7] op_sel_hi:[1,0]
	v_pk_mul_f32 v[18:19], v[18:19], s[6:7] op_sel_hi:[1,0]
	global_store_dwordx2 v[106:107], v[42:43], off offset:128
	v_cvt_u32_f32_e32 v38, v38
	v_cvt_u32_f32_e32 v35, v35
	v_max_u32_e32 v42, 1, v34
	v_max_u32_e32 v34, 1, v39
	v_fma_f32 v39, v40, s33, 0.5
	v_fma_f32 v36, v36, s33, 0.5
	v_fma_f32 v40, v41, s33, 0.5
	v_fma_f32 v37, v37, s33, 0.5
	v_exp_f32_e32 v22, v22
	v_exp_f32_e32 v18, v18
	v_exp_f32_e32 v23, v23
	v_exp_f32_e32 v19, v19
	v_cvt_u32_f32_e32 v39, v39
	v_cvt_u32_f32_e32 v36, v36
	v_cvt_u32_f32_e32 v40, v40
	v_cvt_u32_f32_e32 v37, v37
	v_pk_add_f32 v[32:33], v[32:33], 1.0 op_sel_hi:[1,0]
	v_pk_add_f32 v[28:29], v[28:29], 1.0 op_sel_hi:[1,0]
	v_rcp_f32_e32 v30, v30
	v_rcp_f32_e32 v27, v27
	v_fma_f32 v26, v26, s33, 0.5
	v_fma_f32 v31, v31, s33, 0.5
	v_rcp_f32_e32 v32, v32
	v_rcp_f32_e32 v28, v28
	v_rcp_f32_e32 v33, v33
	v_rcp_f32_e32 v29, v29
	v_cvt_u32_f32_e32 v26, v26
	v_cvt_u32_f32_e32 v31, v31
	v_pk_add_f32 v[24:25], v[24:25], v[136:137]
	v_pk_add_f32 v[20:21], v[20:21], v[132:133]
	v_max_u32_e32 v38, 1, v38
	v_max_u32_e32 v35, 1, v35
	v_pk_mul_f32 v[24:25], v[24:25], s[6:7] op_sel_hi:[1,0]
	v_pk_mul_f32 v[20:21], v[20:21], s[6:7] op_sel_hi:[1,0]
	v_pk_add_f32 v[22:23], v[22:23], 1.0 op_sel_hi:[1,0]
	v_pk_add_f32 v[18:19], v[18:19], 1.0 op_sel_hi:[1,0]
	v_max_u32_sdwa v39, v39, v228 dst_sel:WORD_1 dst_unused:UNUSED_PAD src0_sel:DWORD src1_sel:DWORD
	v_max_u32_sdwa v36, v36, v228 dst_sel:WORD_1 dst_unused:UNUSED_PAD src0_sel:DWORD src1_sel:DWORD
	v_max_u32_sdwa v40, v40, v228 dst_sel:BYTE_3 dst_unused:UNUSED_PAD src0_sel:DWORD src1_sel:DWORD
	v_max_u32_sdwa v37, v37, v228 dst_sel:BYTE_3 dst_unused:UNUSED_PAD src0_sel:DWORD src1_sel:DWORD
	v_lshl_or_b32 v34, v34, 8, v38
	v_lshl_or_b32 v35, v35, 8, v42
	v_exp_f32_e32 v24, v24
	v_exp_f32_e32 v25, v25
	v_exp_f32_e32 v20, v20
	v_exp_f32_e32 v21, v21
	v_rcp_f32_e32 v18, v18
	v_rcp_f32_e32 v23, v23
	v_pk_add_f32 v[14:15], v[14:15], v[134:135]
	v_pk_add_f32 v[10:11], v[10:11], v[130:131]
	v_or3_b32 v34, v34, v39, v40
	v_or3_b32 v35, v35, v36, v37
	v_fma_f32 v30, v30, s33, 0.5
	v_fma_f32 v27, v27, s33, 0.5
	v_pk_mul_f32 v[14:15], v[14:15], s[6:7] op_sel_hi:[1,0]
	v_pk_mul_f32 v[10:11], v[10:11], s[6:7] op_sel_hi:[1,0]
	global_store_dwordx2 v[98:99], v[34:35], off offset:128
	v_cvt_u32_f32_e32 v30, v30
	v_cvt_u32_f32_e32 v27, v27
	v_max_u32_e32 v34, 1, v26
	v_max_u32_e32 v26, 1, v31
	v_fma_f32 v31, v32, s33, 0.5
	v_fma_f32 v28, v28, s33, 0.5
	v_fma_f32 v32, v33, s33, 0.5
	v_fma_f32 v29, v29, s33, 0.5
	v_exp_f32_e32 v14, v14
	v_exp_f32_e32 v10, v10
	v_exp_f32_e32 v15, v15
	v_exp_f32_e32 v11, v11
	v_cvt_u32_f32_e32 v31, v31
	v_cvt_u32_f32_e32 v28, v28
	v_cvt_u32_f32_e32 v32, v32
	v_cvt_u32_f32_e32 v29, v29
	v_pk_add_f32 v[24:25], v[24:25], 1.0 op_sel_hi:[1,0]
	v_pk_add_f32 v[20:21], v[20:21], 1.0 op_sel_hi:[1,0]
	v_rcp_f32_e32 v22, v22
	v_rcp_f32_e32 v19, v19
	v_fma_f32 v18, v18, s33, 0.5
	v_fma_f32 v23, v23, s33, 0.5
	v_rcp_f32_e32 v24, v24
	v_rcp_f32_e32 v20, v20
	v_rcp_f32_e32 v25, v25
	v_rcp_f32_e32 v21, v21
	v_cvt_u32_f32_e32 v18, v18
	v_cvt_u32_f32_e32 v23, v23
	v_pk_add_f32 v[16:17], v[16:17], v[136:137]
	v_pk_add_f32 v[12:13], v[12:13], v[132:133]
	v_max_u32_e32 v30, 1, v30
	v_max_u32_e32 v27, 1, v27
	v_pk_mul_f32 v[16:17], v[16:17], s[6:7] op_sel_hi:[1,0]
	v_pk_mul_f32 v[12:13], v[12:13], s[6:7] op_sel_hi:[1,0]
	v_pk_add_f32 v[14:15], v[14:15], 1.0 op_sel_hi:[1,0]
	v_pk_add_f32 v[10:11], v[10:11], 1.0 op_sel_hi:[1,0]
	v_max_u32_sdwa v31, v31, v228 dst_sel:WORD_1 dst_unused:UNUSED_PAD src0_sel:DWORD src1_sel:DWORD
	v_max_u32_sdwa v28, v28, v228 dst_sel:WORD_1 dst_unused:UNUSED_PAD src0_sel:DWORD src1_sel:DWORD
	v_max_u32_sdwa v32, v32, v228 dst_sel:BYTE_3 dst_unused:UNUSED_PAD src0_sel:DWORD src1_sel:DWORD
	v_max_u32_sdwa v29, v29, v228 dst_sel:BYTE_3 dst_unused:UNUSED_PAD src0_sel:DWORD src1_sel:DWORD
;     __device__ __forceinline__ void operator()(const AccT& acc, const gm::GUnit& u, int wr, int wc, int fr, int fq) const {
;     ...
;             for (int bj = 0; bj < 2; ++bj) {
;                 const f32x4 b0 = bb[bj][0], b1 = bb[bj][1];
; #pragma unroll
;                 for (int ai = 0; ai < 2; ++ai)
; #pragma unroll
;                     for (int m = 0; m < 4; ++m) {
;                         const int row = u.pm * 256 + ai * 128 + wr * 64 + m * 16 + fr;
;                         f32x4 v0 = (acc[ai][bj][m][0] + b0) * -1.4426950408889634f, v1 = (acc[ai][bj][m][1] + b1) * -1.4426950408889634f;
; #pragma unroll
;                         for (int j = 0; j < 4; ++j) { v0[j] = __builtin_amdgcn_exp2f(v0[j]); v1[j] = __builtin_amdgcn_exp2f(v1[j]); }
;                         v0 = v0 + 1.f; v1 = v1 + 1.f;
; #pragma unroll
;                         for (int j = 0; j < 4; ++j) { v0[j] = __builtin_amdgcn_rcpf(v0[j]); v1[j] = __builtin_amdgcn_rcpf(v1[j]); }
;                         v0 = v0 * 255.f + 0.5f; v1 = v1 * 255.f + 0.5f;
;                         unsigned q[8];
; #pragma unroll
;                         for (int j = 0; j < 4; ++j) { q[j] = max((unsigned)v0[j], 1u); q[4 + j] = max((unsigned)v1[j], 1u); }
;                         u32x2 w; w.x = q[0] | (q[1] << 8) | (q[2] << 16) | (q[3] << 24); w.y = q[4] | (q[5] << 8) | (q[6] << 16) | (q[7] << 24);
;                         *(u32x2*)(G8 + (size_t)row * INW + u.pn * 256 + bj * 128 + wc * 32 + 8 * fq) = w;
;                     }
	v_lshl_or_b32 v26, v26, 8, v30
	v_lshl_or_b32 v27, v27, 8, v34
	v_exp_f32_e32 v16, v16
	v_exp_f32_e32 v17, v17
	v_exp_f32_e32 v12, v12
	v_exp_f32_e32 v13, v13
	v_rcp_f32_e32 v10, v10
	v_rcp_f32_e32 v15, v15
	v_pk_add_f32 v[6:7], v[6:7], v[134:135]
	v_pk_add_f32 v[2:3], v[2:3], v[130:131]
	v_or3_b32 v26, v26, v31, v32
	v_or3_b32 v27, v27, v28, v29
	v_fma_f32 v22, v22, s33, 0.5
	v_fma_f32 v19, v19, s33, 0.5
	v_pk_mul_f32 v[6:7], v[6:7], s[6:7] op_sel_hi:[1,0]
	v_pk_mul_f32 v[2:3], v[2:3], s[6:7] op_sel_hi:[1,0]
	global_store_dwordx2 v[90:91], v[26:27], off offset:128
	v_cvt_u32_f32_e32 v22, v22
	v_cvt_u32_f32_e32 v19, v19
	v_max_u32_e32 v26, 1, v18
	v_max_u32_e32 v18, 1, v23
	v_fma_f32 v23, v24, s33, 0.5
	v_fma_f32 v20, v20, s33, 0.5
	v_fma_f32 v24, v25, s33, 0.5
	v_fma_f32 v21, v21, s33, 0.5
	v_exp_f32_e32 v6, v6
	v_exp_f32_e32 v2, v2
	v_exp_f32_e32 v7, v7
	v_exp_f32_e32 v3, v3
	v_cvt_u32_f32_e32 v23, v23
	v_cvt_u32_f32_e32 v20, v20
	v_cvt_u32_f32_e32 v24, v24
	v_cvt_u32_f32_e32 v21, v21
	v_pk_add_f32 v[16:17], v[16:17], 1.0 op_sel_hi:[1,0]
	v_pk_add_f32 v[12:13], v[12:13], 1.0 op_sel_hi:[1,0]
	v_rcp_f32_e32 v14, v14
	v_rcp_f32_e32 v11, v11
	v_fma_f32 v10, v10, s33, 0.5
	v_fma_f32 v15, v15, s33, 0.5
	v_rcp_f32_e32 v16, v16
	v_rcp_f32_e32 v12, v12
	v_rcp_f32_e32 v17, v17
	v_rcp_f32_e32 v13, v13
	v_cvt_u32_f32_e32 v10, v10
	v_cvt_u32_f32_e32 v15, v15
	v_pk_add_f32 v[8:9], v[8:9], v[136:137]
	v_pk_add_f32 v[4:5], v[4:5], v[132:133]
	v_max_u32_e32 v22, 1, v22
	v_max_u32_e32 v19, 1, v19
	v_pk_mul_f32 v[8:9], v[8:9], s[6:7] op_sel_hi:[1,0]
	v_pk_mul_f32 v[4:5], v[4:5], s[6:7] op_sel_hi:[1,0]
	v_pk_add_f32 v[6:7], v[6:7], 1.0 op_sel_hi:[1,0]
	v_pk_add_f32 v[2:3], v[2:3], 1.0 op_sel_hi:[1,0]
	v_max_u32_sdwa v23, v23, v228 dst_sel:WORD_1 dst_unused:UNUSED_PAD src0_sel:DWORD src1_sel:DWORD
	v_max_u32_sdwa v20, v20, v228 dst_sel:WORD_1 dst_unused:UNUSED_PAD src0_sel:DWORD src1_sel:DWORD
	v_max_u32_sdwa v24, v24, v228 dst_sel:BYTE_3 dst_unused:UNUSED_PAD src0_sel:DWORD src1_sel:DWORD
	v_max_u32_sdwa v21, v21, v228 dst_sel:BYTE_3 dst_unused:UNUSED_PAD src0_sel:DWORD src1_sel:DWORD
	v_lshl_or_b32 v18, v18, 8, v22
	v_lshl_or_b32 v19, v19, 8, v26
	v_exp_f32_e32 v8, v8
	v_exp_f32_e32 v9, v9
	v_exp_f32_e32 v4, v4
	v_exp_f32_e32 v5, v5
	v_rcp_f32_e32 v2, v2
	v_rcp_f32_e32 v7, v7
	v_or3_b32 v18, v18, v23, v24
	v_or3_b32 v19, v19, v20, v21
	v_fma_f32 v14, v14, s33, 0.5
	v_fma_f32 v11, v11, s33, 0.5
	global_store_dwordx2 v[82:83], v[18:19], off offset:128
	v_cvt_u32_f32_e32 v14, v14
	v_cvt_u32_f32_e32 v11, v11
	v_max_u32_e32 v18, 1, v10
	v_max_u32_e32 v10, 1, v15
	v_fma_f32 v15, v16, s33, 0.5
	v_fma_f32 v12, v12, s33, 0.5
	v_fma_f32 v16, v17, s33, 0.5
	v_fma_f32 v13, v13, s33, 0.5
	v_cvt_u32_f32_e32 v15, v15
	v_cvt_u32_f32_e32 v12, v12
	v_cvt_u32_f32_e32 v16, v16
	v_cvt_u32_f32_e32 v13, v13
	v_pk_add_f32 v[8:9], v[8:9], 1.0 op_sel_hi:[1,0]
	v_pk_add_f32 v[4:5], v[4:5], 1.0 op_sel_hi:[1,0]
	v_rcp_f32_e32 v6, v6
	v_rcp_f32_e32 v3, v3
	v_fma_f32 v2, v2, s33, 0.5
	v_fma_f32 v7, v7, s33, 0.5
	v_rcp_f32_e32 v8, v8
	v_rcp_f32_e32 v4, v4
	v_rcp_f32_e32 v9, v9
	v_rcp_f32_e32 v5, v5
	v_cvt_u32_f32_e32 v2, v2
	v_cvt_u32_f32_e32 v7, v7
	v_max_u32_e32 v14, 1, v14
	v_max_u32_e32 v11, 1, v11
	v_max_u32_sdwa v15, v15, v228 dst_sel:WORD_1 dst_unused:UNUSED_PAD src0_sel:DWORD src1_sel:DWORD
	v_max_u32_sdwa v12, v12, v228 dst_sel:WORD_1 dst_unused:UNUSED_PAD src0_sel:DWORD src1_sel:DWORD
	v_max_u32_sdwa v16, v16, v228 dst_sel:BYTE_3 dst_unused:UNUSED_PAD src0_sel:DWORD src1_sel:DWORD
	v_max_u32_sdwa v13, v13, v228 dst_sel:BYTE_3 dst_unused:UNUSED_PAD src0_sel:DWORD src1_sel:DWORD
	v_lshl_or_b32 v10, v10, 8, v14
	v_lshl_or_b32 v11, v11, 8, v18
	v_or3_b32 v10, v10, v15, v16
	v_or3_b32 v11, v11, v12, v13
	v_fma_f32 v6, v6, s33, 0.5
	v_fma_f32 v3, v3, s33, 0.5
	global_store_dwordx2 v[74:75], v[10:11], off offset:128
	v_cvt_u32_f32_e32 v6, v6
	v_cvt_u32_f32_e32 v3, v3
	v_max_u32_e32 v10, 1, v2
	v_max_u32_e32 v2, 1, v7
	v_fma_f32 v7, v8, s33, 0.5
	v_fma_f32 v4, v4, s33, 0.5
	v_fma_f32 v8, v9, s33, 0.5
	v_fma_f32 v5, v5, s33, 0.5
	v_cvt_u32_f32_e32 v7, v7
	v_cvt_u32_f32_e32 v4, v4
	v_cvt_u32_f32_e32 v8, v8
	v_cvt_u32_f32_e32 v5, v5
	v_max_u32_e32 v6, 1, v6
	v_max_u32_e32 v3, 1, v3
	v_max_u32_sdwa v7, v7, v228 dst_sel:WORD_1 dst_unused:UNUSED_PAD src0_sel:DWORD src1_sel:DWORD
	v_max_u32_sdwa v4, v4, v228 dst_sel:WORD_1 dst_unused:UNUSED_PAD src0_sel:DWORD src1_sel:DWORD
	v_max_u32_sdwa v8, v8, v228 dst_sel:BYTE_3 dst_unused:UNUSED_PAD src0_sel:DWORD src1_sel:DWORD
	v_max_u32_sdwa v5, v5, v228 dst_sel:BYTE_3 dst_unused:UNUSED_PAD src0_sel:DWORD src1_sel:DWORD
	v_lshl_or_b32 v2, v2, 8, v6
	v_lshl_or_b32 v3, v3, 8, v10
	v_or3_b32 v2, v2, v7, v8
	v_or3_b32 v3, v3, v4, v5
	global_store_dwordx2 v[66:67], v[2:3], off offset:128
	s_branch .LBB0_237
